# M1: baseline + K3 l1-loss hoisted under the main load batch + K1 unit swap (co-resident blocks share gh)
# baseline (speedup 1.0000x reference)
amdhsa.kernels:
  - .agpr_count:     0
    .args:
      - .actual_access:  read_only
        .address_space:  global
        .offset:         0
        .size:           8
        .value_kind:     global_buffer
      - .actual_access:  read_only
        .address_space:  global
        .offset:         8
        .size:           8
        .value_kind:     global_buffer
      - .actual_access:  read_only
        .address_space:  global
        .offset:         16
        .size:           8
        .value_kind:     global_buffer
      - .actual_access:  write_only
        .address_space:  global
        .offset:         24
        .size:           8
        .value_kind:     global_buffer
      - .actual_access:  write_only
        .address_space:  global
        .offset:         32
        .size:           8
        .value_kind:     global_buffer
      - .actual_access:  write_only
        .address_space:  global
        .offset:         40
        .size:           8
        .value_kind:     global_buffer
    .group_segment_fixed_size: 57344
    .kernarg_segment_align: 8
    .kernarg_segment_size: 48
    .language:       OpenCL C
    .language_version:
      - 2
      - 0
    .max_flat_workgroup_size: 512
    .name:           _Z12gemm1_kernelPKfS0_S0_PDv8_DF16_PDF16_S3_
    .private_segment_fixed_size: 0
    .sgpr_count:     18
    .sgpr_spill_count: 0
    .symbol:         _Z12gemm1_kernelPKfS0_S0_PDv8_DF16_PDF16_S3_.kd
    .uniform_work_group_size: 1
    .uses_dynamic_stack: false
    .vgpr_count:     125
    .vgpr_spill_count: 0
    .wavefront_size: 64
  - .agpr_count:     0
    .args:
      - .actual_access:  read_only
        .address_space:  global
        .offset:         0
        .size:           8
        .value_kind:     global_buffer
      - .actual_access:  read_only
        .address_space:  global
        .offset:         8
        .size:           8
        .value_kind:     global_buffer
      - .actual_access:  read_only
        .address_space:  global
        .offset:         16
        .size:           8
        .value_kind:     global_buffer
      - .actual_access:  read_only
        .address_space:  global
        .offset:         24
        .size:           8
        .value_kind:     global_buffer
      - .actual_access:  write_only
        .address_space:  global
        .offset:         32
        .size:           8
        .value_kind:     global_buffer
      - .actual_access:  write_only
        .address_space:  global
        .offset:         40
        .size:           8
        .value_kind:     global_buffer
    .group_segment_fixed_size: 87040
    .kernarg_segment_align: 8
    .kernarg_segment_size: 48
    .language:       OpenCL C
    .language_version:
      - 2
      - 0
    .max_flat_workgroup_size: 768
    .name:           _Z11attn_kernelPKiPKDv8_DF16_PKDF16_S5_PDF16_Pf
    .private_segment_fixed_size: 0
    .sgpr_count:     55
    .sgpr_spill_count: 0
    .symbol:         _Z11attn_kernelPKiPKDv8_DF16_PKDF16_S5_PDF16_Pf.kd
    .uniform_work_group_size: 1
    .uses_dynamic_stack: false
    .vgpr_count:     156
    .vgpr_spill_count: 0
    .wavefront_size: 64
  - .agpr_count:     12
    .args:
      - .actual_access:  read_only
        .address_space:  global
        .offset:         0
        .size:           8
        .value_kind:     global_buffer
      - .actual_access:  read_only
        .address_space:  global
        .offset:         8
        .size:           8
        .value_kind:     global_buffer
      - .actual_access:  read_only
        .address_space:  global
        .offset:         16
        .size:           8
        .value_kind:     global_buffer
      - .actual_access:  read_only
        .address_space:  global
        .offset:         24
        .size:           8
        .value_kind:     global_buffer
      - .actual_access:  read_only
        .address_space:  global
        .offset:         32
        .size:           8
        .value_kind:     global_buffer
      - .actual_access:  read_only
        .address_space:  global
        .offset:         40
        .size:           8
        .value_kind:     global_buffer
      - .actual_access:  write_only
        .address_space:  global
        .offset:         48
        .size:           8
        .value_kind:     global_buffer
    .group_segment_fixed_size: 16192
    .kernarg_segment_align: 8
    .kernarg_segment_size: 56
    .language:       OpenCL C
    .language_version:
      - 2
      - 0
    .max_flat_workgroup_size: 256
    .name:           _Z10epi_kernelPKDF16_PKfS2_S2_S2_S2_Pf
    .private_segment_fixed_size: 0
    .sgpr_count:     38
    .sgpr_spill_count: 0
    .symbol:         _Z10epi_kernelPKDF16_PKfS2_S2_S2_S2_Pf.kd
    .uniform_work_group_size: 1
    .uses_dynamic_stack: false
    .vgpr_count:     140
    .vgpr_spill_count: 0
    .wavefront_size: 64
